# speedup vs baseline: 1.1025x; 1.0056x over previous
.LBB0_7:
	s_or_b64 exec, exec, s[4:5]
	s_mov_b32 s34, 0x60441c00
	v_writelane_b32 v20, s34, 0
	s_mov_b32 s34, 0x53371d01
	v_writelane_b32 v20, s34, 1
	s_mov_b32 s34, 0x62461e02
	v_writelane_b32 v20, s34, 2
	s_mov_b32 s34, 0x6f471f03
	v_writelane_b32 v20, s34, 3
	s_mov_b32 s34, 0x78522a0e
	v_writelane_b32 v20, s34, 4
	s_mov_b32 s34, 0x61452b0f
	v_writelane_b32 v20, s34, 5
	s_mov_b32 s34, 0x6e543810
	v_writelane_b32 v20, s34, 6
	s_mov_b32 s34, 0x78553911
	v_writelane_b32 v20, s34, 7
	s_mov_b32 s34, 0x70482c12
	v_writelane_b32 v20, s34, 8
	s_mov_b32 s34, 0x71573b13
	v_writelane_b32 v20, s34, 9
	s_mov_b32 s34, 0x78643c14
	v_writelane_b32 v20, s34, 10
	s_mov_b32 s34, 0x734b2f15
	v_writelane_b32 v20, s34, 11
	s_mov_b32 s34, 0x563a2004
	v_writelane_b32 v20, s34, 12
	s_mov_b32 s34, 0x63492d05
	v_writelane_b32 v20, s34, 13
	s_mov_b32 s34, 0x724a2e06
	v_writelane_b32 v20, s34, 14
	s_mov_b32 s34, 0x653d2107
	v_writelane_b32 v20, s34, 15
	s_mov_b32 s34, 0x74583e22
	v_writelane_b32 v20, s34, 16
	s_mov_b32 s34, 0x78673f23
	v_writelane_b32 v20, s34, 17
	s_mov_b32 s34, 0x765a3216
	v_writelane_b32 v20, s34, 18
	s_mov_b32 s34, 0x775b4125
	v_writelane_b32 v20, s34, 19
	s_mov_b32 s34, 0x664c3008
	v_writelane_b32 v20, s34, 20
	s_mov_b32 s34, 0x75593109
	v_writelane_b32 v20, s34, 21
	s_mov_b32 s34, 0x6840240a
	v_writelane_b32 v20, s34, 22
	s_mov_b32 s34, 0x694d3317
	v_writelane_b32 v20, s34, 23
	s_mov_b32 s34, 0x785c3418
	v_writelane_b32 v20, s34, 24
	s_mov_b32 s34, 0x6b4f270b
	v_writelane_b32 v20, s34, 25
	s_mov_b32 s34, 0x5e42280c
	v_writelane_b32 v20, s34, 26
	s_mov_b32 s34, 0x6d51290d
	v_writelane_b32 v20, s34, 27
	s_mov_b32 s34, 0x786a4e26
	v_writelane_b32 v20, s34, 28
	s_mov_b32 s34, 0x785d3519
	v_writelane_b32 v20, s34, 29
	s_mov_b32 s34, 0x6c50361a
	v_writelane_b32 v20, s34, 30
	s_mov_b32 s34, 0x785f431b
	v_writelane_b32 v20, s34, 31
	s_add_u32 s32, s20, s30
	s_addc_u32 s33, s21, 0
	v_lshlrev_b32_e32 v21, 2, v0
	v_add_u32_e32 v21, 0x21000, v21
	v_cmp_gt_u32_e32 vcc, 32, v0
	s_and_saveexec_b64 s[4:5], vcc
	global_store_dword v21, v20, s[32:33]
	s_or_b64 exec, exec, s[4:5]
	s_mov_b64 s[4:5], 0

.LBB1_4:
	s_or_b64 exec, exec, s[22:23]
	s_load_dwordx4 s[68:71], s[0:1], 0x8
	s_load_dwordx2 s[4:5], s[0:1], 0x18
	s_and_b32 s22, s2, 7
	s_bfe_u32 s66, s3, 0x20006
	s_lshr_b32 s67, s3, 8
	s_mul_i32 s33, s22, 0x30000
	s_waitcnt lgkmcnt(0)
	s_add_u32 s22, s4, s33
	s_addc_u32 s23, s5, 0
	s_add_u32 s4, s68, s33
	s_addc_u32 s5, s69, 0
	s_add_u32 s34, s70, s33
	s_addc_u32 s35, s71, 0
	s_lshl_b32 s68, s66, 6
	s_mul_i32 s69, s67, 0x900
	v_and_b32_e32 v100, 63, v0
	s_or_b32 s64, s68, s69
	v_or_b32_e32 v2, s64, v100
	s_add_i32 s65, s64, 0x100
	v_ashrrev_i32_e32 v3, 31, v2
	v_or_b32_e32 v4, s65, v100
	v_lshl_add_u64 v[2:3], v[2:3], 4, s[22:23]
	v_ashrrev_i32_e32 v5, 31, v4
	s_add_i32 s65, s64, 0x200
	v_lshl_add_u64 v[4:5], v[4:5], 4, s[22:23]
	global_load_dwordx4 v[82:85], v[2:3], off
	global_load_dwordx4 v[74:77], v[4:5], off
	v_or_b32_e32 v2, s65, v100
	s_add_i32 s65, s64, 0x300
	v_ashrrev_i32_e32 v3, 31, v2
	v_or_b32_e32 v4, s65, v100
	v_lshl_add_u64 v[2:3], v[2:3], 4, s[22:23]
	v_ashrrev_i32_e32 v5, 31, v4
	s_addk_i32 s64, 0x400
	v_lshl_add_u64 v[4:5], v[4:5], 4, s[22:23]
	global_load_dwordx4 v[78:81], v[2:3], off
	global_load_dwordx4 v[70:73], v[4:5], off
	v_or_b32_e32 v2, s64, v100
	v_ashrrev_i32_e32 v3, 31, v2
	v_lshl_add_u64 v[2:3], v[2:3], 4, s[22:23]
	v_mov_b32_e32 v99, 0
	v_lshlrev_b32_e32 v98, 4, v100
	global_load_dwordx4 v[66:69], v[2:3], off
	s_add_i32 s65, s64, 0x100
	v_or_b32_e32 v2, s65, v100
	v_mov_b32_e32 v3, 0
	v_lshl_add_u64 v[2:3], v[2:3], 4, s[22:23]
	global_load_dwordx4 v[108:111], v[2:3], off
	s_add_i32 s65, s64, 0x200
	v_or_b32_e32 v2, s65, v100
	v_mov_b32_e32 v3, 0
	v_lshl_add_u64 v[2:3], v[2:3], 4, s[22:23]
	global_load_dwordx4 v[118:121], v[2:3], off
	s_add_i32 s65, s64, 0x300
	v_or_b32_e32 v2, s65, v100
	v_mov_b32_e32 v3, 0
	v_lshl_add_u64 v[2:3], v[2:3], 4, s[22:23]
	global_load_dwordx4 v[122:125], v[2:3], off
	v_and_b32_e32 v117, 31, v0
	v_lshlrev_b32_e32 v117, 2, v117
	v_add_u32_e32 v117, 0x21000, v117
	global_load_dword v117, v117, s[22:23]
	v_bfe_u32 v115, v0, 5, 1
	s_cmp_gt_u32 s3, 63
	s_cselect_b64 s[34:35], -1, 0
	s_and_b64 vcc, exec, s[34:35]
	s_cbranch_vccz .LBB1_46
	v_cmp_gt_u32_e64 s[4:5], 21, v0
	v_lshlrev_b32_e32 v1, 2, v0
	s_and_saveexec_b64 s[64:65], s[4:5]
	s_cbranch_execnz .LBB1_47

.LBB1_15:
	s_or_b64 exec, exec, s[12:13]
	v_and_b32_e32 v114, 31, v0
	s_mul_i32 s9, s67, 0x60
	v_or_b32_e32 v15, s9, v114
	v_min_u32_e32 v91, 0xa8, v15
	v_mul_lo_u16_e32 v15, 0x4f, v91
	s_lshl_b32 s7, s66, 3
	v_lshrrev_b16_e32 v15, 9, v15
	s_or_b32 s8, s7, 0xb600
	v_and_b32_e32 v15, 62, v15
	v_add_u32_e32 v15, v91, v15
	s_movk_i32 s6, 0x48
	v_mov_b32_e32 v99, s8
	v_mad_u32_u24 v42, v15, s6, v99
	v_mad_u32_u24 v43, v115, s6, v42
	s_waitcnt lgkmcnt(0)
	s_barrier
	ds_read2_b64 v[34:37], v43 offset1:1
	ds_read2_b64 v[38:41], v43 offset0:135 offset1:136
	v_mov_b32_e32 v2, v46
	v_mov_b32_e32 v3, v46
	v_mov_b32_e32 v4, v46
	v_mov_b32_e32 v5, v46
	v_mov_b32_e32 v6, v47
	v_mov_b32_e32 v7, v47
	v_mov_b32_e32 v8, v47
	v_mov_b32_e32 v9, v47
	v_mov_b32_e32 v10, v48
	v_mov_b32_e32 v11, v48
	v_mov_b32_e32 v12, v48
	v_mov_b32_e32 v13, v48
	v_mov_b32_e32 v14, v49
	v_mov_b32_e32 v15, v49
	v_mov_b32_e32 v16, v49
	v_mov_b32_e32 v17, v49
	s_movk_i32 s8, 0x438
	s_add_i32 s12, s9, 32
	s_waitcnt lgkmcnt(1)
	v_mfma_f32_32x32x16_f16 v[18:33], v[86:89], v[34:37], v[2:17]
	v_add_u32_e32 v34, 0x8b8, v43
	ds_read2_b64 v[34:37], v34 offset1:1
	v_and_or_b32 v107, v0, 32, s7
	s_movk_i32 s7, 0x110
	v_mad_u32_u24 v91, v91, s7, v107
	s_add_i32 s9, s9, 64
	s_lshr_b32 s42, s3, 6
	s_waitcnt lgkmcnt(1)
	v_mfma_f32_32x32x16_f16 v[18:33], v[62:65], v[38:41], v[18:33]
	v_mad_u32_u24 v38, v115, s8, v42
	ds_read2_b64 v[38:41], v38 offset0:18 offset1:19
	s_cmpk_lt_u32 s3, 0x100
	s_cselect_b64 s[30:31], -1, 0
	s_add_i32 s13, s69, 0x600
	s_add_i32 s14, s69, 0x700
	v_lshlrev_b32_e32 v116, 4, v115
	s_waitcnt lgkmcnt(1)
	v_mfma_f32_32x32x16_f16 v[18:33], v[58:61], v[34:37], v[18:33]
	v_add_u32_e32 v34, 0x870, v43
	ds_read2_b64 v[34:37], v34 offset1:1
	s_movk_i32 s15, 0x1070
	s_movk_i32 s16, 0x1ba0
	s_movk_i32 s17, 0x1c20
	s_waitcnt lgkmcnt(1)
	v_mfma_f32_32x32x16_f16 v[18:33], v[54:57], v[38:41], v[18:33]
	v_or_b32_e32 v38, s12, v114
	v_min_u32_e32 v101, 0xa8, v38
	v_mul_lo_u16_e32 v38, 0x4f, v101
	v_lshrrev_b16_e32 v38, 9, v38
	v_and_b32_e32 v38, 62, v38
	v_add_u32_e32 v38, v101, v38
	v_mad_u32_u24 v97, v38, s6, v99
	v_mad_u32_u24 v106, v115, s6, v97
	ds_read2_b64 v[92:95], v106 offset1:1
	v_add_u32_e32 v96, 0x8b8, v106
	ds_read2_b64 v[102:105], v96 offset1:1
	s_waitcnt lgkmcnt(2)
	v_mfma_f32_32x32x16_f16 v[18:33], v[50:53], v[34:37], v[18:33]
	s_add_i32 s12, s69, 0x500
	s_addk_i32 s69, 0x800
	s_cmpk_gt_u32 s3, 0xff
	s_cselect_b64 vcc, -1, 0
	s_waitcnt lgkmcnt(1)
	v_mfma_f32_32x32x16_f16 v[34:49], v[86:89], v[92:95], v[2:17]
	ds_read2_b64 v[92:95], v106 offset0:135 offset1:136
	s_nop 4
	v_cvt_pk_f16_f32 v18, v18, v19
	v_pk_max_f16 v96, v18, 0
	v_mad_u32_u24 v18, v115, s8, v97
	v_cvt_pk_f16_f32 v22, v22, v23
	v_add_u32_e32 v23, 0x870, v106
	v_cvt_pk_f16_f32 v30, v30, v31
	s_waitcnt lgkmcnt(0)
	v_mfma_f32_32x32x16_f16 v[34:49], v[62:65], v[92:95], v[34:49]
	v_cvt_pk_f16_f32 v92, v20, v21
	ds_read2_b64 v[18:21], v18 offset0:18 offset1:19
	v_pk_max_f16 v97, v92, 0
	ds_read2_b64 v[92:95], v23 offset1:1
	v_cvt_pk_f16_f32 v31, v32, v33
	v_mfma_f32_32x32x16_f16 v[34:49], v[58:61], v[102:105], v[34:49]
	v_or_b32_e32 v102, 64, v114
	s_waitcnt lgkmcnt(1)
	v_mfma_f32_32x32x16_f16 v[34:49], v[54:57], v[18:21], v[34:49]
	v_cvt_pk_f16_f32 v19, v24, v25
	v_pk_max_f16 v18, v22, 0
	v_pk_max_f16 v19, v19, 0
	ds_write2_b64 v91, v[96:97], v[18:19] offset1:8
	v_cvt_pk_f16_f32 v18, v26, v27
	v_pk_max_f16 v26, v18, 0
	v_or_b32_e32 v18, s9, v114
	v_cvt_pk_f16_f32 v22, v28, v29
	v_min_u32_e32 v28, 0xa8, v18
	v_mul_lo_u16_e32 v18, 0x4f, v28
	v_lshrrev_b16_e32 v18, 9, v18
	v_and_b32_e32 v18, 62, v18
	v_add_u32_e32 v18, v28, v18
	v_mad_u32_u24 v29, v18, s6, v99
	s_waitcnt lgkmcnt(1)
	v_mfma_f32_32x32x16_f16 v[34:49], v[50:53], v[92:95], v[34:49]
	v_add_u32_e32 v94, s68, v100
	v_add_u32_e32 v94, s69, v94
	v_mov_b32_e32 v95, 0
	v_lshl_add_u64 v[94:95], v[94:95], 4, s[22:23]
	global_load_dwordx4 v[94:97], v[94:95], off
	v_mad_u32_u24 v92, v115, s6, v29
	ds_read2_b64 v[18:21], v92 offset1:1
	v_pk_max_f16 v27, v22, 0
	ds_read2_b64 v[22:25], v92 offset0:135 offset1:136
	v_or_b32_e32 v99, 32, v114
	s_nop 6
	v_cvt_pk_f16_f32 v32, v40, v41
	s_waitcnt lgkmcnt(1)
	v_mfma_f32_32x32x16_f16 v[2:17], v[86:89], v[18:21], v[2:17]
	v_pk_max_f16 v18, v30, 0
	v_pk_max_f16 v19, v31, 0
	ds_write2_b64 v91, v[26:27], v[18:19] offset0:16 offset1:24
	v_cvt_pk_f16_f32 v18, v34, v35
	v_cvt_pk_f16_f32 v19, v36, v37
	v_pk_max_f16 v26, v18, 0
	v_add_u32_e32 v18, 0x8b8, v92
	s_waitcnt lgkmcnt(1)
	v_mfma_f32_32x32x16_f16 v[2:17], v[62:65], v[22:25], v[2:17]
	v_pk_max_f16 v27, v19, 0
	ds_read2_b64 v[18:21], v18 offset1:1
	v_mad_u32_u24 v22, v115, s8, v29
	ds_read2_b64 v[22:25], v22 offset0:18 offset1:19
	v_cvt_pk_f16_f32 v31, v38, v39
	v_mad_u32_u24 v30, v101, s7, v107
	s_and_b64 s[8:9], vcc, exec
	s_waitcnt lgkmcnt(1)
	v_mfma_f32_32x32x16_f16 v[2:17], v[58:61], v[18:21], v[2:17]
	v_pk_max_f16 v18, v31, 0
	v_pk_max_f16 v19, v32, 0
	ds_write2_b64 v30, v[26:27], v[18:19] offset1:8
	v_cvt_pk_f16_f32 v18, v42, v43
	v_cvt_pk_f16_f32 v19, v44, v45
	v_pk_max_f16 v26, v18, 0
	v_add_u32_e32 v18, 0x870, v92
	s_waitcnt lgkmcnt(1)
	v_mfma_f32_32x32x16_f16 v[2:17], v[54:57], v[22:25], v[2:17]
	v_pk_max_f16 v27, v19, 0
	ds_read2_b64 v[18:21], v18 offset1:1
	v_cvt_pk_f16_f32 v22, v46, v47
	v_cvt_pk_f16_f32 v23, v48, v49
	v_pk_max_f16 v22, v22, 0
	v_pk_max_f16 v23, v23, 0
	ds_write2_b64 v30, v[26:27], v[22:23] offset0:16 offset1:24
	s_waitcnt lgkmcnt(1)
	v_mfma_f32_32x32x16_f16 v[2:17], v[50:53], v[18:21], v[2:17]
	v_mad_u32_u24 v18, v28, s7, v107
	v_lshl_or_b32 v42, s66, 5, v116
	s_cselect_b32 s8, 0xf60, 0
	s_movk_i32 s9, 0xff0
	s_cselect_b32 s9, s9, 0x80
	s_cselect_b32 s15, s15, 0x110
	s_cselect_b32 s16, s16, 0x190
	s_nop 4
	v_cvt_pk_f16_f32 v2, v2, v3
	v_cvt_pk_f16_f32 v3, v4, v5
	v_cvt_pk_f16_f32 v4, v6, v7
	v_cvt_pk_f16_f32 v5, v8, v9
	v_pk_max_f16 v2, v2, 0
	v_pk_max_f16 v3, v3, 0
	v_pk_max_f16 v4, v4, 0
	v_pk_max_f16 v5, v5, 0
	ds_write2_b64 v18, v[2:3], v[4:5] offset1:8
	v_cvt_pk_f16_f32 v2, v10, v11
	v_cvt_pk_f16_f32 v3, v12, v13
	v_cvt_pk_f16_f32 v4, v14, v15
	v_cvt_pk_f16_f32 v5, v16, v17
	v_pk_max_f16 v2, v2, 0
	v_pk_max_f16 v3, v3, 0
	v_pk_max_f16 v4, v4, 0
	v_pk_max_f16 v5, v5, 0
	ds_write2_b64 v18, v[2:3], v[4:5] offset0:16 offset1:24
	s_waitcnt vmcnt(0)
	v_bfe_u32 v2, v117, 0, 8
	v_mul_u32_u24_e32 v3, 0xbb, v2
	v_lshrrev_b32_e32 v3, 11, v3
	v_lshl_add_u32 v103, v3, 1, v2
	v_bfe_u32 v2, v117, 8, 8
	v_mul_u32_u24_e32 v3, 0xbb, v2
	v_lshrrev_b32_e32 v3, 11, v3
	v_lshl_add_u32 v106, v3, 1, v2
	v_mad_u32_u24 v90, v103, s7, v42
	v_mad_u32_u24 v91, v106, s7, v42
	v_add_u32_e32 v2, s8, v90
	v_add_u32_e32 v6, s8, v91
	s_waitcnt lgkmcnt(0)
	s_barrier
	ds_read_b128 v[2:5], v2
	ds_read_b128 v[6:9], v6
	s_waitcnt lgkmcnt(1)
	v_mfma_f32_32x32x16_f16 v[18:33], v[82:85], v[2:5], 0
	v_add_u32_e32 v34, s9, v90
	v_add_u32_e32 v38, s9, v91
	ds_read_b128 v[34:37], v34
	ds_read_b128 v[38:41], v38
	s_cselect_b32 s17, s17, 0x220
	v_or_b32_e32 v101, 0x60, v114
	s_waitcnt lgkmcnt(2)
	v_mfma_f32_32x32x16_f16 v[2:17], v[82:85], v[6:9], 0
	s_waitcnt lgkmcnt(1)
	v_mfma_f32_32x32x16_f16 v[18:33], v[74:77], v[34:37], v[18:33]
	v_add_u32_e32 v34, s15, v90
	ds_read_b128 v[34:37], v34
	s_waitcnt lgkmcnt(1)
	v_mfma_f32_32x32x16_f16 v[2:17], v[74:77], v[38:41], v[2:17]
	v_add_u32_e32 v38, s15, v91
	ds_read_b128 v[38:41], v38
	s_waitcnt lgkmcnt(1)
	v_mfma_f32_32x32x16_f16 v[18:33], v[78:81], v[34:37], v[18:33]
	v_add_u32_e32 v34, s16, v90
	ds_read_b128 v[34:37], v34
	s_waitcnt lgkmcnt(1)
	v_mfma_f32_32x32x16_f16 v[2:17], v[78:81], v[38:41], v[2:17]
	v_add_u32_e32 v38, s16, v91
	ds_read_b128 v[38:41], v38
	s_waitcnt lgkmcnt(1)
	v_mfma_f32_32x32x16_f16 v[18:33], v[70:73], v[34:37], v[18:33]
	v_bfe_u32 v43, v117, 16, 8
	v_mul_u32_u24_e32 v34, 0xbb, v43
	v_lshrrev_b32_e32 v104, 11, v34
	v_add_u32_e32 v34, s17, v90
	ds_read_b128 v[34:37], v34
	v_lshl_add_u32 v104, v104, 1, v43
	v_mad_u32_u24 v92, v104, s7, v42
	s_waitcnt lgkmcnt(1)
	v_mfma_f32_32x32x16_f16 v[2:17], v[70:73], v[38:41], v[2:17]
	v_add_u32_e32 v38, s17, v91
	ds_read_b128 v[38:41], v38
	s_waitcnt lgkmcnt(1)
	v_mfma_f32_32x32x16_f16 v[18:33], v[66:69], v[34:37], v[18:33]
	v_bfe_u32 v34, v117, 24, 8
	v_mul_u32_u24_e32 v35, 0xbb, v34
	v_lshrrev_b32_e32 v35, 11, v35
	v_lshl_add_u32 v105, v35, 1, v34
	v_mad_u32_u24 v93, v105, s7, v42
	s_waitcnt lgkmcnt(0)
	v_mfma_f32_32x32x16_f16 v[2:17], v[66:69], v[38:41], v[2:17]
	v_add_u32_e32 v34, s8, v92
	v_add_u32_e32 v38, s8, v93
	ds_read_b128 v[34:37], v34
	ds_read_b128 v[38:41], v38
	v_add_u32_e32 v86, s9, v93
	s_waitcnt lgkmcnt(1)
	v_mfma_f32_32x32x16_f16 v[50:65], v[82:85], v[34:37], 0
	ds_read_b128 v[86:89], v86
	s_waitcnt lgkmcnt(1)
	v_mfma_f32_32x32x16_f16 v[34:49], v[82:85], v[38:41], 0
	v_add_u32_e32 v82, s9, v92
	ds_read_b128 v[82:85], v82
	s_waitcnt lgkmcnt(0)
	v_mfma_f32_32x32x16_f16 v[50:65], v[74:77], v[82:85], v[50:65]
	v_add_u32_e32 v82, s15, v93
	ds_read_b128 v[82:85], v82
	v_mfma_f32_32x32x16_f16 v[34:49], v[74:77], v[86:89], v[34:49]
	v_add_u32_e32 v74, s15, v92
	ds_read_b128 v[74:77], v74
	s_waitcnt lgkmcnt(0)
	v_mfma_f32_32x32x16_f16 v[50:65], v[78:81], v[74:77], v[50:65]
	v_add_u32_e32 v74, s16, v92
	ds_read_b128 v[74:77], v74
	v_mfma_f32_32x32x16_f16 v[34:49], v[78:81], v[82:85], v[34:49]
	v_add_u32_e32 v78, s16, v93
	ds_read_b128 v[78:81], v78
	s_waitcnt lgkmcnt(1)
	v_mfma_f32_32x32x16_f16 v[50:65], v[70:73], v[74:77], v[50:65]
	v_add_u32_e32 v74, s17, v93
	ds_read_b128 v[74:77], v74
	s_waitcnt lgkmcnt(1)
	v_mfma_f32_32x32x16_f16 v[34:49], v[70:73], v[78:81], v[34:49]
	v_add_u32_e32 v70, s17, v92
	ds_read_b128 v[70:73], v70
	s_waitcnt lgkmcnt(0)
	v_mfma_f32_32x32x16_f16 v[50:65], v[66:69], v[70:73], v[50:65]
	v_mfma_f32_32x32x16_f16 v[34:49], v[66:69], v[74:77], v[34:49]
	s_movk_i32 s7, 0x1cb0
	s_cselect_b32 s7, s7, 0x2a0
	v_add_u32_e32 v74, s7, v90
	ds_read_b128 v[74:77], v74
	v_add_u32_e32 v78, s7, v91
	ds_read_b128 v[78:81], v78
	s_movk_i32 s12, 0x1d30
	s_cselect_b32 s12, s12, 0xdd0
	s_movk_i32 s8, 0x1dc0
	s_cselect_b32 s8, s8, 0xe50
	s_movk_i32 s9, 0x1e40
	s_cselect_b32 s9, s9, 0xee0
	s_waitcnt vmcnt(0) lgkmcnt(1)
	v_mfma_f32_32x32x16_f16 v[18:33], v[108:111], v[74:77], v[18:33]
	v_add_u32_e32 v82, s12, v91
	ds_read_b128 v[82:85], v82
	s_waitcnt lgkmcnt(1)
	v_mfma_f32_32x32x16_f16 v[2:17], v[108:111], v[78:81], v[2:17]
	v_add_u32_e32 v78, s12, v90
	ds_read_b128 v[78:81], v78
	s_waitcnt lgkmcnt(0)
	v_mfma_f32_32x32x16_f16 v[18:33], v[118:121], v[78:81], v[18:33]
	v_add_u32_e32 v86, s8, v91
	ds_read_b128 v[86:89], v86
	v_mfma_f32_32x32x16_f16 v[2:17], v[118:121], v[82:85], v[2:17]
	v_add_u32_e32 v82, s8, v90
	ds_read_b128 v[82:85], v82
	s_waitcnt lgkmcnt(0)
	v_mfma_f32_32x32x16_f16 v[18:33], v[122:125], v[82:85], v[18:33]
	v_add_u32_e32 v82, s9, v90
	ds_read_b128 v[82:85], v82
	v_mfma_f32_32x32x16_f16 v[2:17], v[122:125], v[86:89], v[2:17]
	v_add_u32_e32 v86, s9, v91
	ds_read_b128 v[86:89], v86
	s_waitcnt lgkmcnt(1)
	v_mfma_f32_32x32x16_f16 v[18:33], v[94:97], v[82:85], v[18:33]
	s_waitcnt lgkmcnt(0)
	v_mfma_f32_32x32x16_f16 v[2:17], v[94:97], v[86:89], v[2:17]
	v_add_u32_e32 v82, s7, v92
	v_add_u32_e32 v86, s7, v93
	ds_read_b128 v[82:85], v82
	ds_read_b128 v[86:89], v86
	s_waitcnt lgkmcnt(1)
	v_mfma_f32_32x32x16_f16 v[50:65], v[108:111], v[82:85], v[50:65]
	v_add_u32_e32 v82, s12, v93
	ds_read_b128 v[82:85], v82
	s_waitcnt lgkmcnt(1)
	v_mfma_f32_32x32x16_f16 v[34:49], v[108:111], v[86:89], v[34:49]
	v_add_u32_e32 v66, s12, v92
	ds_read_b128 v[66:69], v66
	s_waitcnt lgkmcnt(0)
	v_mfma_f32_32x32x16_f16 v[50:65], v[118:121], v[66:69], v[50:65]
	v_add_u32_e32 v66, s8, v92
	ds_read_b128 v[66:69], v66
	v_mfma_f32_32x32x16_f16 v[34:49], v[118:121], v[82:85], v[34:49]
	v_add_u32_e32 v70, s8, v93
	ds_read_b128 v[70:73], v70
	s_waitcnt lgkmcnt(1)
	v_mfma_f32_32x32x16_f16 v[50:65], v[122:125], v[66:69], v[50:65]
	v_add_u32_e32 v66, s9, v92
	ds_read_b128 v[66:69], v66
	s_waitcnt lgkmcnt(1)
	v_mfma_f32_32x32x16_f16 v[34:49], v[122:125], v[70:73], v[34:49]
	v_add_u32_e32 v70, s9, v93
	ds_read_b128 v[70:73], v70
	s_waitcnt lgkmcnt(1)
	v_mfma_f32_32x32x16_f16 v[50:65], v[94:97], v[66:69], v[50:65]
	s_waitcnt lgkmcnt(0)
	v_mfma_f32_32x32x16_f16 v[34:49], v[94:97], v[70:73], v[34:49]
	s_cmpk_gt_u32 s3, 0x17f
	s_barrier
	s_cbranch_scc1 .LBB1_17
	s_mul_hi_u32 s7, s42, 0x55555556
	s_mul_i32 s7, s7, 3
	s_sub_i32 s7, s42, s7
	s_lshl_b32 s7, s7, 3
	s_add_i32 s8, s7, 0xb600
	s_cmpk_gt_u32 s3, 0xbf
	s_cselect_b32 s9, 0x60, 0
	s_movk_i32 s12, 0x438
	s_movk_i32 s13, 0xd0
	v_mad_u32_u24 v99, v115, 24, s7
	v_add_u32_e32 v122, 0xf550, v98
	ds_read_b128 v[82:85], v98 offset:62800
	ds_read_b128 v[86:89], v98 offset:63824
	ds_read_b128 v[90:93], v98 offset:64848
	ds_read_b128 v[94:97], v122 offset:3072
	ds_read_b128 v[118:121], v122 offset:4096
	ds_read_b32 v107, v122 offset:5120
	ds_read_b32 v112, v122 offset:5124
	ds_read_b32 v113, v122 offset:5128
	ds_read_b32 v117, v122 offset:5132
	v_or_b32_e32 v101, s9, v114
	v_min_u32_e32 v101, 0xa8, v101
	v_mul_lo_u16_e32 v102, 0x4f, v101
	v_lshrrev_b16_e32 v102, 9, v102
	v_and_b32_e32 v102, 62, v102
	v_add_u32_e32 v102, v101, v102
	v_mov_b32_e32 v123, s8
	v_mad_u32_u24 v102, v102, s6, v123
	v_mad_u32_u24 v123, v115, s6, v102
	v_mad_u32_u24 v102, v115, s12, v102
	v_mad_u32_u24 v101, v101, s13, v99
	ds_read2_b64 v[108:111], v123 offset0:4 offset1:5
	ds_read2_b64 v[124:127], v123 offset0:139 offset1:140
	v_add_u32_e32 v122, 0x8d8, v123
	s_waitcnt lgkmcnt(1)
	v_mfma_f32_32x32x16_f16 v[66:81], v[82:85], v[108:111], 0
	ds_read2_b64 v[108:111], v122 offset1:1
	v_add_u32_e32 v122, 0x890, v123
	s_waitcnt lgkmcnt(1)
	v_mfma_f32_32x32x16_f16 v[66:81], v[86:89], v[124:127], v[66:81]
	ds_read2_b64 v[124:127], v102 offset0:22 offset1:23
	s_waitcnt lgkmcnt(1)
	v_mfma_f32_32x32x16_f16 v[66:81], v[90:93], v[108:111], v[66:81]
	ds_read2_b64 v[108:111], v122 offset1:1
	s_waitcnt lgkmcnt(1)
	v_mfma_f32_32x32x16_f16 v[66:81], v[94:97], v[124:127], v[66:81]
	s_waitcnt lgkmcnt(0)
	v_mfma_f32_32x32x16_f16 v[66:81], v[118:121], v[108:111], v[66:81]
	s_add_i32 s14, s9, 32
	v_or_b32_e32 v124, s14, v114
	v_min_u32_e32 v124, 0xa8, v124
	v_mul_lo_u16_e32 v126, 0x4f, v124
	v_lshrrev_b16_e32 v126, 9, v126
	v_and_b32_e32 v126, 62, v126
	v_add_u32_e32 v126, v124, v126
	v_mov_b32_e32 v123, s8
	v_mad_u32_u24 v126, v126, s6, v123
	v_mad_u32_u24 v123, v115, s6, v126
	v_mad_u32_u24 v102, v115, s12, v126
	v_mad_u32_u24 v125, v124, s13, v99
	ds_read2_b64 v[108:111], v123 offset0:4 offset1:5
	v_add_f32_e32 v66, v107, v66
	v_add_f32_e32 v67, v107, v67
	v_add_f32_e32 v68, v107, v68
	v_add_f32_e32 v69, v107, v69
	v_add_f32_e32 v70, v112, v70
	v_add_f32_e32 v71, v112, v71
	v_add_f32_e32 v72, v112, v72
	v_add_f32_e32 v73, v112, v73
	v_add_f32_e32 v74, v113, v74
	v_add_f32_e32 v75, v113, v75
	v_add_f32_e32 v76, v113, v76
	v_add_f32_e32 v77, v113, v77
	v_add_f32_e32 v78, v117, v78
	v_add_f32_e32 v79, v117, v79
	v_add_f32_e32 v80, v117, v80
	v_add_f32_e32 v81, v117, v81
	v_cvt_pk_f16_f32 v66, v66, v67
	v_cvt_pk_f16_f32 v67, v68, v69
	v_cvt_pk_f16_f32 v68, v70, v71
	v_cvt_pk_f16_f32 v69, v72, v73
	v_cvt_pk_f16_f32 v70, v74, v75
	v_cvt_pk_f16_f32 v71, v76, v77
	v_cvt_pk_f16_f32 v72, v78, v79
	v_cvt_pk_f16_f32 v73, v80, v81
	v_pk_max_f16 v66, v66, 0
	v_pk_max_f16 v67, v67, 0
	v_pk_max_f16 v68, v68, 0
	v_pk_max_f16 v69, v69, 0
	v_pk_max_f16 v70, v70, 0
	v_pk_max_f16 v71, v71, 0
	v_pk_max_f16 v72, v72, 0
	v_pk_max_f16 v73, v73, 0
	ds_write2_b64 v101, v[66:67], v[68:69] offset1:6
	ds_write2_b64 v101, v[70:71], v[72:73] offset0:12 offset1:18
	v_mov_b32_e32 v101, v125
	ds_read2_b64 v[124:127], v123 offset0:139 offset1:140
	v_add_u32_e32 v122, 0x8d8, v123
	s_waitcnt lgkmcnt(1)
	v_mfma_f32_32x32x16_f16 v[66:81], v[82:85], v[108:111], 0
	ds_read2_b64 v[108:111], v122 offset1:1
	v_add_u32_e32 v122, 0x890, v123
	s_waitcnt lgkmcnt(1)
	v_mfma_f32_32x32x16_f16 v[66:81], v[86:89], v[124:127], v[66:81]
	ds_read2_b64 v[124:127], v102 offset0:22 offset1:23
	s_waitcnt lgkmcnt(1)
	v_mfma_f32_32x32x16_f16 v[66:81], v[90:93], v[108:111], v[66:81]
	ds_read2_b64 v[108:111], v122 offset1:1
	s_waitcnt lgkmcnt(1)
	v_mfma_f32_32x32x16_f16 v[66:81], v[94:97], v[124:127], v[66:81]
	s_waitcnt lgkmcnt(0)
	v_mfma_f32_32x32x16_f16 v[66:81], v[118:121], v[108:111], v[66:81]
	s_add_i32 s14, s9, 64
	v_or_b32_e32 v124, s14, v114
	v_min_u32_e32 v124, 0xa8, v124
	v_mul_lo_u16_e32 v126, 0x4f, v124
	v_lshrrev_b16_e32 v126, 9, v126
	v_and_b32_e32 v126, 62, v126
	v_add_u32_e32 v126, v124, v126
	v_mov_b32_e32 v123, s8
	v_mad_u32_u24 v126, v126, s6, v123
	v_mad_u32_u24 v123, v115, s6, v126
	v_mad_u32_u24 v102, v115, s12, v126
	v_mad_u32_u24 v125, v124, s13, v99
	ds_read2_b64 v[108:111], v123 offset0:4 offset1:5
	v_add_f32_e32 v66, v107, v66
	v_add_f32_e32 v67, v107, v67
	v_add_f32_e32 v68, v107, v68
	v_add_f32_e32 v69, v107, v69
	v_add_f32_e32 v70, v112, v70
	v_add_f32_e32 v71, v112, v71
	v_add_f32_e32 v72, v112, v72
	v_add_f32_e32 v73, v112, v73
	v_add_f32_e32 v74, v113, v74
	v_add_f32_e32 v75, v113, v75
	v_add_f32_e32 v76, v113, v76
	v_add_f32_e32 v77, v113, v77
	v_add_f32_e32 v78, v117, v78
	v_add_f32_e32 v79, v117, v79
	v_add_f32_e32 v80, v117, v80
	v_add_f32_e32 v81, v117, v81
	v_cvt_pk_f16_f32 v66, v66, v67
	v_cvt_pk_f16_f32 v67, v68, v69
	v_cvt_pk_f16_f32 v68, v70, v71
	v_cvt_pk_f16_f32 v69, v72, v73
	v_cvt_pk_f16_f32 v70, v74, v75
	v_cvt_pk_f16_f32 v71, v76, v77
	v_cvt_pk_f16_f32 v72, v78, v79
	v_cvt_pk_f16_f32 v73, v80, v81
	v_pk_max_f16 v66, v66, 0
	v_pk_max_f16 v67, v67, 0
	v_pk_max_f16 v68, v68, 0
	v_pk_max_f16 v69, v69, 0
	v_pk_max_f16 v70, v70, 0
	v_pk_max_f16 v71, v71, 0
	v_pk_max_f16 v72, v72, 0
	v_pk_max_f16 v73, v73, 0
	ds_write2_b64 v101, v[66:67], v[68:69] offset1:6
	ds_write2_b64 v101, v[70:71], v[72:73] offset0:12 offset1:18
	v_mov_b32_e32 v101, v125
	ds_read2_b64 v[124:127], v123 offset0:139 offset1:140
	v_add_u32_e32 v122, 0x8d8, v123
	s_waitcnt lgkmcnt(1)
	v_mfma_f32_32x32x16_f16 v[66:81], v[82:85], v[108:111], 0
	ds_read2_b64 v[108:111], v122 offset1:1
	v_add_u32_e32 v122, 0x890, v123
	s_waitcnt lgkmcnt(1)
	v_mfma_f32_32x32x16_f16 v[66:81], v[86:89], v[124:127], v[66:81]
	ds_read2_b64 v[124:127], v102 offset0:22 offset1:23
	s_waitcnt lgkmcnt(1)
	v_mfma_f32_32x32x16_f16 v[66:81], v[90:93], v[108:111], v[66:81]
	ds_read2_b64 v[108:111], v122 offset1:1
	s_waitcnt lgkmcnt(1)
	v_mfma_f32_32x32x16_f16 v[66:81], v[94:97], v[124:127], v[66:81]
	s_waitcnt lgkmcnt(0)
	v_mfma_f32_32x32x16_f16 v[66:81], v[118:121], v[108:111], v[66:81]
	v_or_b32_e32 v99, 32, v114
	v_or_b32_e32 v102, 64, v114
	s_nop 9
	v_add_f32_e32 v66, v107, v66
	v_add_f32_e32 v67, v107, v67
	v_add_f32_e32 v68, v107, v68
	v_add_f32_e32 v69, v107, v69
	v_add_f32_e32 v70, v112, v70
	v_add_f32_e32 v71, v112, v71
	v_add_f32_e32 v72, v112, v72
	v_add_f32_e32 v73, v112, v73
	v_add_f32_e32 v74, v113, v74
	v_add_f32_e32 v75, v113, v75
	v_add_f32_e32 v76, v113, v76
	v_add_f32_e32 v77, v113, v77
	v_add_f32_e32 v78, v117, v78
	v_add_f32_e32 v79, v117, v79
	v_add_f32_e32 v80, v117, v80
	v_add_f32_e32 v81, v117, v81
	v_cvt_pk_f16_f32 v66, v66, v67
	v_cvt_pk_f16_f32 v67, v68, v69
	v_cvt_pk_f16_f32 v68, v70, v71
	v_cvt_pk_f16_f32 v69, v72, v73
	v_cvt_pk_f16_f32 v70, v74, v75
	v_cvt_pk_f16_f32 v71, v76, v77
	v_cvt_pk_f16_f32 v72, v78, v79
	v_cvt_pk_f16_f32 v73, v80, v81
	v_pk_max_f16 v66, v66, 0
	v_pk_max_f16 v67, v67, 0
	v_pk_max_f16 v68, v68, 0
	v_pk_max_f16 v69, v69, 0
	v_pk_max_f16 v70, v70, 0
	v_pk_max_f16 v71, v71, 0
	v_pk_max_f16 v72, v72, 0
	v_pk_max_f16 v73, v73, 0
	ds_write2_b64 v101, v[66:67], v[68:69] offset1:6
	ds_write2_b64 v101, v[70:71], v[72:73] offset0:12 offset1:18
	v_or_b32_e32 v101, 0x60, v114
.LBB1_17:
	v_lshlrev_b32_e32 v107, 2, v114
	v_add_u32_e32 v107, 0x21000, v107
	global_load_dword v107, v107, s[22:23]
	s_mul_i32 s16, s66, 15
	s_lshl_b32 s14, s67, 3
	s_addk_i32 s16, 0x48
	s_add_i32 s6, s16, s14
	s_lshl_b32 s6, s6, 6
	v_or_b32_e32 v66, s6, v100
	v_mov_b32_e32 v67, 0
	v_lshl_add_u64 v[68:69], v[66:67], 4, s[22:23]
	global_load_dwordx4 v[70:73], v[68:69], off
	s_add_i32 s7, s6, 64
	v_or_b32_e32 v66, s7, v100
	v_lshl_add_u64 v[68:69], v[66:67], 4, s[22:23]
	global_load_dwordx4 v[74:77], v[68:69], off
	s_add_i32 s7, s6, 0x80
	v_or_b32_e32 v66, s7, v100
	v_lshl_add_u64 v[68:69], v[66:67], 4, s[22:23]
	global_load_dwordx4 v[78:81], v[68:69], off
	s_addk_i32 s6, 0xc0
	v_or_b32_e32 v66, s6, v100
	v_lshl_add_u64 v[68:69], v[66:67], 4, s[22:23]
	global_load_dwordx4 v[82:85], v[68:69], off
	s_add_i32 s7, s6, 64
	v_or_b32_e32 v66, s7, v100
	v_lshl_add_u64 v[68:69], v[66:67], 4, s[22:23]
	global_load_dwordx4 v[108:111], v[68:69], off
	s_add_i32 s7, s6, 0x80
	v_or_b32_e32 v66, s7, v100
	v_lshl_add_u64 v[68:69], v[66:67], 4, s[22:23]
	global_load_dwordx4 v[118:121], v[68:69], off
	s_add_i32 s7, s6, 0xc0
	v_or_b32_e32 v66, s7, v100
	v_lshl_add_u64 v[68:69], v[66:67], 4, s[22:23]
	global_load_dwordx4 v[122:125], v[68:69], off
	s_and_b64 s[74:75], vcc, exec
	s_movk_i32 s7, 0x100
	s_cselect_b32 s7, 0xc0, s7
	s_add_i32 s7, s6, s7
	v_or_b32_e32 v66, s7, v100
	v_lshl_add_u64 v[112:113], v[66:67], 4, s[22:23]
	s_mul_i32 s66, s66, 48
	v_mul_u32_u24_e32 v69, 0xd0, v115
	v_mul_u32_u24_e32 v66, 0xd0, v103
	v_mul_u32_u24_e32 v86, 0xd0, v106
	s_movk_i32 s8, 0x9c0
	v_add3_u32 v68, v66, s66, v69
	v_add3_u32 v66, v86, s66, v69
	v_mad_u32_u24 v94, v115, s8, v68
	s_and_b64 s[6:7], vcc, exec
	v_mad_u32_u24 v96, v115, s8, v66
	v_cndmask_b32_e32 v95, v68, v94, vcc
	s_cselect_b32 s6, 0x1b0, 0
	v_cndmask_b32_e32 v97, v66, v96, vcc
	v_add_u32_e32 v86, s6, v95
	v_add_u32_e32 v90, s6, v97
	s_waitcnt lgkmcnt(0)
	s_barrier
	ds_read_b128 v[86:89], v86
	ds_read_b128 v[90:93], v90
	s_movk_i32 s7, 0x1530
	s_cselect_b32 s7, s7, 0xa90
	s_cselect_b32 s9, 32, 0x15f0
	s_movk_i32 s12, 0xab0
	s_cselect_b32 s12, s12, 0x1a0
	s_waitcnt vmcnt(6) lgkmcnt(1)
	v_mfma_f32_32x32x16_f16 v[18:33], v[70:73], v[86:89], v[18:33]
	v_add_u32_e32 v86, s7, v68
	ds_read_b128 v[86:89], v86
	s_waitcnt lgkmcnt(1)
	v_mfma_f32_32x32x16_f16 v[2:17], v[70:73], v[90:93], v[2:17]
	v_add_u32_e32 v90, s7, v66
	ds_read_b128 v[90:93], v90
	s_waitcnt vmcnt(5) lgkmcnt(1)
	v_mfma_f32_32x32x16_f16 v[18:33], v[74:77], v[86:89], v[18:33]
	v_add_u32_e32 v86, s9, v68
	ds_read_b128 v[86:89], v86
	s_waitcnt lgkmcnt(1)
	v_mfma_f32_32x32x16_f16 v[2:17], v[74:77], v[90:93], v[2:17]
	v_add_u32_e32 v90, s9, v66
	ds_read_b128 v[90:93], v90
	s_waitcnt vmcnt(4) lgkmcnt(1)
	v_mfma_f32_32x32x16_f16 v[18:33], v[78:81], v[86:89], v[18:33]
	v_cndmask_b32_e32 v86, v94, v68, vcc
	v_add_u32_e32 v86, s12, v86
	ds_read_b128 v[86:89], v86
	s_waitcnt lgkmcnt(1)
	v_mfma_f32_32x32x16_f16 v[2:17], v[78:81], v[90:93], v[2:17]
	v_cndmask_b32_e32 v90, v96, v66, vcc
	v_add_u32_e32 v90, s12, v90
	ds_read_b128 v[90:93], v90
	s_waitcnt vmcnt(3) lgkmcnt(1)
	v_mfma_f32_32x32x16_f16 v[18:33], v[82:85], v[86:89], v[18:33]
	v_mul_u32_u24_e32 v86, 0xd0, v104
	v_mul_u32_u24_e32 v87, 0xd0, v105
	v_add3_u32 v94, v86, s66, v69
	v_add3_u32 v69, v87, s66, v69
	v_mad_u32_u24 v96, v115, s8, v94
	v_mad_u32_u24 v103, v115, s8, v69
	s_waitcnt lgkmcnt(0)
	v_mfma_f32_32x32x16_f16 v[2:17], v[82:85], v[90:93], v[2:17]
	v_cndmask_b32_e32 v104, v94, v96, vcc
	v_cndmask_b32_e32 v105, v69, v103, vcc
	v_add_u32_e32 v86, s6, v104
	v_add_u32_e32 v90, s6, v105
	ds_read_b128 v[86:89], v86
	ds_read_b128 v[90:93], v90
	s_waitcnt lgkmcnt(1)
	v_mfma_f32_32x32x16_f16 v[50:65], v[70:73], v[86:89], v[50:65]
	v_add_u32_e32 v86, s7, v69
	ds_read_b128 v[86:89], v86
	s_waitcnt lgkmcnt(1)
	v_mfma_f32_32x32x16_f16 v[34:49], v[70:73], v[90:93], v[34:49]
	v_add_u32_e32 v70, s7, v94
	ds_read_b128 v[70:73], v70
	s_waitcnt lgkmcnt(0)
	v_mfma_f32_32x32x16_f16 v[50:65], v[74:77], v[70:73], v[50:65]
	v_add_u32_e32 v70, s9, v94
	ds_read_b128 v[70:73], v70
	v_mfma_f32_32x32x16_f16 v[34:49], v[74:77], v[86:89], v[34:49]
	global_load_dwordx4 v[86:89], v[112:113], off
	v_add_u32_e32 v74, s9, v69
	ds_read_b128 v[74:77], v74
	s_waitcnt lgkmcnt(1)
	v_mfma_f32_32x32x16_f16 v[50:65], v[78:81], v[70:73], v[50:65]
	v_cndmask_b32_e32 v70, v96, v94, vcc
	v_add_u32_e32 v70, s12, v70
	ds_read_b128 v[70:73], v70
	s_waitcnt lgkmcnt(1)
	v_mfma_f32_32x32x16_f16 v[34:49], v[78:81], v[74:77], v[34:49]
	v_cndmask_b32_e32 v74, v103, v69, vcc
	v_add_u32_e32 v74, s12, v74
	ds_read_b128 v[74:77], v74
	s_waitcnt lgkmcnt(1)
	v_mfma_f32_32x32x16_f16 v[50:65], v[82:85], v[70:73], v[50:65]
	s_waitcnt lgkmcnt(0)
	v_mfma_f32_32x32x16_f16 v[34:49], v[82:85], v[74:77], v[34:49]
	s_movk_i32 s24, 0x1610
	s_and_b64 s[16:17], vcc, exec
	s_cselect_b32 s16, s24, 0x1520
	v_add_u32_e32 v78, s16, v68
	ds_read_b128 v[78:81], v78
	v_add_u32_e32 v82, s16, v66
	ds_read_b128 v[82:85], v82
	s_cselect_b32 s6, 0x1c0, 16
	s_movk_i32 s7, 0x1540
	s_cselect_b32 s7, s7, 0xaa0
	s_movk_i32 s8, 0x1600
	s_cselect_b32 s8, 0x1540, s8
	s_waitcnt vmcnt(3) lgkmcnt(1)
	v_mfma_f32_32x32x16_f16 v[18:33], v[108:111], v[78:81], v[18:33]
	v_add_u32_e32 v70, s6, v95
	ds_read_b128 v[70:73], v70
	s_waitcnt lgkmcnt(1)
	v_mfma_f32_32x32x16_f16 v[2:17], v[108:111], v[82:85], v[2:17]
	v_add_u32_e32 v82, s6, v97
	ds_read_b128 v[82:85], v82
	s_waitcnt vmcnt(2) lgkmcnt(1)
	v_mfma_f32_32x32x16_f16 v[18:33], v[118:121], v[70:73], v[18:33]
	v_add_u32_e32 v90, s7, v68
	ds_read_b128 v[90:93], v90
	v_add_u32_e32 v68, s8, v68
	s_waitcnt lgkmcnt(1)
	v_mfma_f32_32x32x16_f16 v[2:17], v[118:121], v[82:85], v[2:17]
	v_add_u32_e32 v82, s7, v66
	ds_read_b128 v[82:85], v82
	v_add_u32_e32 v66, s8, v66
	s_waitcnt vmcnt(0) lgkmcnt(1)
	v_mfma_f32_32x32x16_f16 v[18:33], v[122:125], v[90:93], v[18:33]
	ds_read_b128 v[90:93], v68
	v_cndmask_b32_e64 v86, v86, 0, vcc
	v_cndmask_b32_e64 v87, v87, 0, vcc
	v_cndmask_b32_e64 v88, v88, 0, vcc
	v_cndmask_b32_e64 v89, v89, 0, vcc
	s_waitcnt lgkmcnt(1)
	v_mfma_f32_32x32x16_f16 v[2:17], v[122:125], v[82:85], v[2:17]
	ds_read_b128 v[82:85], v66
	s_waitcnt lgkmcnt(1)
	v_mfma_f32_32x32x16_f16 v[18:33], v[86:89], v[90:93], v[18:33]
	s_waitcnt lgkmcnt(0)
	v_mfma_f32_32x32x16_f16 v[2:17], v[86:89], v[82:85], v[2:17]
	v_add_u32_e32 v70, s16, v94
	v_add_u32_e32 v74, s16, v69
	ds_read_b128 v[70:73], v70
	ds_read_b128 v[74:77], v74
	s_waitcnt lgkmcnt(1)
	v_mfma_f32_32x32x16_f16 v[50:65], v[108:111], v[70:73], v[50:65]
	v_add_u32_e32 v70, s6, v104
	ds_read_b128 v[70:73], v70
	s_waitcnt lgkmcnt(1)
	v_mfma_f32_32x32x16_f16 v[34:49], v[108:111], v[74:77], v[34:49]
	v_add_u32_e32 v74, s6, v105
	ds_read_b128 v[74:77], v74
	s_waitcnt lgkmcnt(1)
	v_mfma_f32_32x32x16_f16 v[50:65], v[118:121], v[70:73], v[50:65]
	v_add_u32_e32 v70, s7, v94
	ds_read_b128 v[70:73], v70
	s_waitcnt lgkmcnt(1)
	v_mfma_f32_32x32x16_f16 v[34:49], v[118:121], v[74:77], v[34:49]
	v_add_u32_e32 v74, s7, v69
	ds_read_b128 v[74:77], v74
	s_waitcnt lgkmcnt(1)
	v_mfma_f32_32x32x16_f16 v[50:65], v[122:125], v[70:73], v[50:65]
	v_add_u32_e32 v70, s8, v94
	ds_read_b128 v[70:73], v70
	s_waitcnt lgkmcnt(1)
	v_mfma_f32_32x32x16_f16 v[34:49], v[122:125], v[74:77], v[34:49]
	v_add_u32_e32 v74, s8, v69
	ds_read_b128 v[74:77], v74
	s_waitcnt lgkmcnt(1)
	v_mfma_f32_32x32x16_f16 v[50:65], v[86:89], v[70:73], v[50:65]
	s_waitcnt lgkmcnt(0)
	v_mfma_f32_32x32x16_f16 v[34:49], v[86:89], v[74:77], v[34:49]
	s_cmpk_lt_i32 s2, 0x200
	s_movk_i32 s8, 0xd3
	s_cselect_b64 s[6:7], -1, 0
	v_cmp_gt_u32_e32 vcc, s8, v0
	s_and_b64 s[8:9], s[6:7], vcc
	s_barrier
	s_and_saveexec_b64 s[6:7], s[8:9]
	s_cbranch_execz .LBB1_19
	s_add_i32 s8, s2, 0x200
	s_mul_hi_i32 s9, s8, 0x6978
	s_mulk_i32 s8, 0x6978
	s_add_u32 s8, s20, s8
	s_addc_u32 s9, s21, s9
	v_lshlrev_b32_e32 v14, 7, v0
	global_load_dword v67, v14, s[8:9]
.LBB1_19:
	s_or_b64 exec, exec, s[6:7]
	s_mul_i32 s9, s42, 0x79
	v_bfe_u32 v15, v107, 0, 8
	v_add_u32_e32 v15, s9, v15
	v_lshlrev_b32_e32 v14, 3, v115
	v_mul_lo_u32 v15, v15, 48
	v_or_b32_e32 v15, v14, v15
	v_cvt_pk_f16_f32 v17, v20, v21
	v_cvt_pk_f16_f32 v16, v18, v19
	v_cvt_pk_f16_f32 v19, v24, v25
	v_cvt_pk_f16_f32 v18, v22, v23
	ds_write2_b64 v15, v[16:17], v[18:19] offset1:2
	v_cvt_pk_f16_f32 v17, v28, v29
	v_cvt_pk_f16_f32 v16, v26, v27
	ds_write_b64 v15, v[16:17] offset:32
	v_bfe_u32 v15, v107, 8, 8
	v_add_u32_e32 v15, s9, v15
	v_mul_lo_u32 v15, v15, 48
	v_or_b32_e32 v15, v14, v15
	v_cvt_pk_f16_f32 v5, v4, v5
	v_cvt_pk_f16_f32 v4, v2, v3
	v_cvt_pk_f16_f32 v3, v8, v9
	v_cvt_pk_f16_f32 v2, v6, v7
	ds_write2_b64 v15, v[4:5], v[2:3] offset1:2
	v_cvt_pk_f16_f32 v3, v12, v13
	v_cvt_pk_f16_f32 v2, v10, v11
	ds_write_b64 v15, v[2:3] offset:32
	v_bfe_u32 v2, v107, 16, 8
	v_add_u32_e32 v2, s9, v2
	v_mul_lo_u32 v2, v2, 48
	s_movk_i32 s8, 0x79
	v_or_b32_e32 v6, v14, v2
	v_cvt_pk_f16_f32 v3, v52, v53
	v_cvt_pk_f16_f32 v2, v50, v51
	v_cvt_pk_f16_f32 v5, v56, v57
	v_cvt_pk_f16_f32 v4, v54, v55
	ds_write2_b64 v6, v[2:3], v[4:5] offset1:2
	v_cvt_pk_f16_f32 v3, v60, v61
	v_cvt_pk_f16_f32 v2, v58, v59
	v_bfe_u32 v15, v107, 24, 8
	v_cmp_gt_u32_e32 vcc, s8, v15
	ds_write_b64 v6, v[2:3] offset:32
	s_and_saveexec_b64 s[6:7], vcc
	s_cbranch_execz .LBB1_21
	v_add_u32_e32 v2, s9, v15
	v_mul_lo_u32 v2, v2, 48
	v_or_b32_e32 v6, v14, v2
	v_cvt_pk_f16_f32 v3, v36, v37
	v_cvt_pk_f16_f32 v2, v34, v35
	v_cvt_pk_f16_f32 v5, v40, v41
	v_cvt_pk_f16_f32 v4, v38, v39
	ds_write2_b64 v6, v[2:3], v[4:5] offset1:2
	v_cvt_pk_f16_f32 v3, v44, v45
	v_cvt_pk_f16_f32 v2, v42, v43
	ds_write_b64 v6, v[2:3] offset:32
